# baseline (speedup 1.0000x reference)
.Lat_spec_ok:
	v_and_b32_e32 v31, 7, v0
	v_bitop3_b32 v33, v10, v0, 7 bitop3:0x78
	v_lshlrev_b32_e32 v1, 7, v1
	v_mbcnt_lo_u32_b32 v34, -1, 0
	v_lshlrev_b32_e32 v89, 4, v33
	v_bitop3_b32 v31, v10, v31, 4 bitop3:0x36
	v_xor_b32_e32 v33, v13, v0
	v_mov_b32_e32 v13, v12
	v_lshlrev_b32_e32 v87, 4, v11
	s_movk_i32 s1, 0x70
	v_lshlrev_b32_e32 v98, 2, v10
	v_mov_b32_e32 v10, v12
	v_mov_b32_e32 v11, v12
	v_mbcnt_hi_u32_b32 v0, -1, v34
	v_lshl_or_b32 v91, v31, 4, v1
	v_lshlrev_b32_e32 v31, 4, v33
	v_mov_b64_e32 v[36:37], v[12:13]
	v_mov_b64_e32 v[40:41], v[12:13]
	v_mov_b64_e32 v[44:45], v[12:13]
	v_mov_b64_e32 v[48:49], v[12:13]
	v_mov_b64_e32 v[52:53], v[12:13]
	s_mov_b32 s17, 0
	v_mov_b64_e32 v[100:101], 0
	s_mov_b64 s[14:15], -1
	s_mov_b32 s5, 0xff800000
	s_mov_b32 s7, 0x41000000
	s_mov_b32 s12, 0x3c003c00
	v_mov_b32_e32 v30, 0x3c003c00
	v_mov_b32_e32 v114, v30
	v_mov_b32_e32 v115, v30
	v_mov_b32_e32 v116, v30
	v_mov_b32_e32 v117, v30
	v_mov_b32_e32 v120, v12
	v_mov_b32_e32 v121, v12
	v_mov_b32_e32 v122, v12
	v_mov_b32_e32 v123, v12
	v_mov_b64_e32 v[34:35], v[10:11]
	v_mov_b64_e32 v[38:39], v[10:11]
	v_mov_b64_e32 v[42:43], v[10:11]
	v_mov_b64_e32 v[46:47], v[10:11]
	v_mov_b64_e32 v[50:51], v[10:11]
	v_and_or_b32 v99, v31, s1, v32
	v_add_u32_e32 v124, v89, v1
	s_mov_b32 s9, 1
	s_waitcnt vmcnt(3)
	ds_write_b128 v99, v[22:25]
	ds_write_b128 v90, v[14:17] offset:8192
	s_waitcnt vmcnt(2)
	ds_write_b128 v99, v[18:21] offset:4096
	s_waitcnt vmcnt(1)
	ds_write_b128 v90, v[26:29] offset:12288
	s_waitcnt vmcnt(0)
	s_cmp_gt_i32 s11, 3
	s_cbranch_scc0 .LBB1_20

.LBB1_27:
	s_waitcnt lgkmcnt(0)
	s_barrier
	s_xor_b32 s9, s9, 1
	s_cmp_lg_u32 s9, 0
	s_cbranch_scc1 .LBB1_27_b
	s_lshl_b32 s13, 1, s0
	s_and_b32 s0, s13, s4
	s_cmp_eq_u32 s0, 0
	s_cbranch_scc1 .LBB1_32
	ds_read_b128 v[58:61], v124
	ds_read_b128 v[62:65], v91
	v_lshrrev_b64 v[10:11], v98, v[102:103]
	v_bfe_i32 v13, v10, 1, 1
	v_bfe_i32 v31, v10, 2, 1
	s_waitcnt lgkmcnt(1)
	v_mfma_f32_16x16x32_f16 v[58:61], v[58:61], v[2:5], v[120:123]
	v_bfe_i32 v32, v10, 3, 1
	v_bfe_i32 v11, v10, 0, 1
	s_waitcnt lgkmcnt(0)
	v_mfma_f32_16x16x32_f16 v[58:61], v[62:65], v[6:9], v[58:61]
	s_nop 7
	v_bitop3_b32 v10, v59, s5, v13 bitop3:0xe4
	v_bitop3_b32 v31, v60, s5, v31 bitop3:0xe4
	v_bitop3_b32 v13, v61, s5, v32 bitop3:0xe4
	v_max_f32_e32 v32, v13, v13
	v_max_f32_e32 v33, v31, v31
	v_bitop3_b32 v11, v58, s5, v11 bitop3:0xe4
	v_max_f32_e32 v32, v33, v32
	v_max3_f32 v32, v11, v10, v32
	v_cmp_lt_f32_e32 vcc, s7, v32
	s_or_b64 s[0:1], s[14:15], vcc
	s_cbranch_scc0 .LBB1_35
	v_and_b32_e32 v58, 64, v0
	v_xor_b32_e32 v33, 16, v0
	v_add_u32_e32 v58, 64, v58
	v_cmp_lt_i32_e32 vcc, v33, v58
	s_mov_b64 s[22:23], 0
	s_nop 0
	v_cndmask_b32_e32 v33, v0, v33, vcc
	v_lshlrev_b32_e32 v33, 2, v33
	ds_bpermute_b32 v33, v33, v32
	v_max_f32_e32 v32, v32, v32
	s_waitcnt lgkmcnt(0)
	v_max_f32_e32 v33, v33, v33
	v_max_f32_e32 v32, v32, v33
	v_mov_b32_e32 v33, v32
	s_nop 1
	v_permlane32_swap_b32_e32 v32, v33
	v_max_f32_e32 v33, v33, v33
	v_max_f32_e32 v32, v32, v32
	v_max_f32_e32 v32, v32, v33
	v_cmp_nlg_f32_e32 vcc, s5, v32
	v_cmp_lg_f32_e64 s[0:1], s5, v32
	s_and_saveexec_b64 s[24:25], s[0:1]
	v_cmp_lt_f32_e64 s[0:1], s7, v32
	s_or_b64 s[0:1], s[14:15], s[0:1]
	s_and_b64 s[22:23], s[0:1], exec
	s_or_b64 exec, exec, s[24:25]
	v_exp_f32_e64 v33, -v32
	v_cndmask_b32_e64 v32, 0, v32, s[22:23]
	v_sub_f32_e32 v11, v11, v32
	v_sub_f32_e32 v10, v10, v32
	v_cndmask_b32_e64 v33, v33, 1.0, s[14:15]
	v_cndmask_b32_e64 v66, 1.0, v33, s[22:23]
	v_pk_mul_f32 v[60:61], v[48:49], v[66:67] op_sel_hi:[1,0]
	v_pk_mul_f32 v[58:59], v[46:47], v[66:67] op_sel_hi:[1,0]
	v_pk_mul_f32 v[64:65], v[66:67], v[44:45] op_sel_hi:[0,1]
	v_pk_mul_f32 v[62:63], v[66:67], v[42:43] op_sel_hi:[0,1]
	v_pk_mul_f32 v[80:81], v[66:67], v[40:41] op_sel_hi:[0,1]
	v_pk_mul_f32 v[78:79], v[66:67], v[38:39] op_sel_hi:[0,1]
	v_pk_mul_f32 v[84:85], v[66:67], v[36:37] op_sel_hi:[0,1]
	v_pk_mul_f32 v[82:83], v[66:67], v[34:35] op_sel_hi:[0,1]
	v_pk_mul_f32 v[68:69], v[52:53], v[66:67] op_sel_hi:[1,0]
	v_pk_mul_f32 v[66:67], v[50:51], v[66:67] op_sel_hi:[1,0]
	v_sub_f32_e32 v31, v31, v32
	v_sub_f32_e32 v13, v13, v32
	v_sub_f32_e32 v120, v120, v32
	v_sub_f32_e32 v121, v121, v32
	v_sub_f32_e32 v122, v122, v32
	v_sub_f32_e32 v123, v123, v32
	s_and_b64 s[0:1], s[14:15], vcc
	s_branch .LBB1_36

.LBB1_34:
	s_waitcnt vmcnt(0)
	v_mov_b64_e32 v[102:103], v[100:101]
	ds_write_b128 v99, v[22:25] offset:16384
	ds_write_b128 v90, v[14:17] offset:24576
	ds_write_b128 v99, v[18:21] offset:20480
	ds_write_b128 v90, v[26:29] offset:28672
	s_cbranch_execnz .LBB1_46
	s_branch .LBB1_47

.LBB1_36:
	v_exp_f32_e32 v31, v31
	v_exp_f32_e32 v13, v13
	ds_read_b128 v[70:73], v87 offset:8192
	v_exp_f32_e32 v74, v11
	v_exp_f32_e32 v10, v10
	v_cvt_pkrtz_f16_f32 v11, v31, v13
	v_cvt_pkrtz_f16_f32 v10, v74, v10
	v_mov_b32_e32 v13, v12
	ds_read_b128 v[108:111], v87 offset:14336
	s_nop 0
	v_mfma_f32_16x16x32_f16 v[74:77], v[114:117], v[10:13], v[66:69]
	s_nop 2
	ds_read_b128 v[66:69], v87 offset:10240
	s_waitcnt lgkmcnt(2)
	v_mfma_f32_16x16x32_f16 v[70:73], v[70:73], v[10:13], v[58:61]
	s_nop 2
	ds_read_b128 v[58:61], v87 offset:12288
	s_waitcnt lgkmcnt(1)
	v_mfma_f32_16x16x32_f16 v[66:69], v[66:69], v[10:13], v[62:65]
	s_waitcnt lgkmcnt(0)
	v_mfma_f32_16x16x32_f16 v[62:65], v[58:61], v[10:13], v[78:81]
	v_mfma_f32_16x16x32_f16 v[58:61], v[108:111], v[10:13], v[82:85]
	s_branch .LBB1_33
.LBB1_37:
	ds_read_b128 v[58:61], v124
	ds_read_b128 v[62:65], v124 offset:2048
	ds_read_b128 v[66:69], v91
	ds_read_b128 v[72:75], v91 offset:2048
	s_and_b32 s0, s13, s6
	s_waitcnt lgkmcnt(3)
	v_mfma_f32_16x16x32_f16 v[58:61], v[58:61], v[2:5], v[120:123]
	s_cmp_lg_u32 s0, 0
	s_waitcnt lgkmcnt(2)
	v_mfma_f32_16x16x32_f16 v[62:65], v[62:65], v[2:5], v[120:123]
	s_waitcnt lgkmcnt(1)
	v_mfma_f32_16x16x32_f16 v[68:71], v[66:69], v[6:9], v[58:61]
	s_waitcnt lgkmcnt(0)
	v_mfma_f32_16x16x32_f16 v[64:67], v[72:75], v[6:9], v[62:65]
	s_nop 0
	ds_read_b128 v[58:61], v124 offset:4096
	ds_read_b128 v[72:75], v124 offset:6144
	ds_read_b128 v[76:79], v91 offset:4096
	ds_read_b128 v[80:83], v91 offset:6144
	s_waitcnt lgkmcnt(3)
	v_mfma_f32_16x16x32_f16 v[58:61], v[58:61], v[2:5], v[120:123]
	s_waitcnt lgkmcnt(1)
	v_mfma_f32_16x16x32_f16 v[60:63], v[76:79], v[6:9], v[58:61]
	v_mfma_f32_16x16x32_f16 v[56:59], v[72:75], v[2:5], v[120:123]
	s_waitcnt lgkmcnt(0)
	v_mfma_f32_16x16x32_f16 v[56:59], v[80:83], v[6:9], v[56:59]
	s_cbranch_scc1 .LBB1_39
	v_lshrrev_b64 v[10:11], v98, v[102:103]
	v_bfe_i32 v13, v10, 0, 1
	v_bitop3_b32 v68, v68, s5, v13 bitop3:0xe4
	v_bfe_i32 v13, v10, 16, 1
	v_bitop3_b32 v64, v64, s5, v13 bitop3:0xe4
	v_bfe_i32 v13, v11, 0, 1
	v_bitop3_b32 v60, v60, s5, v13 bitop3:0xe4
	v_bfe_i32 v13, v11, 16, 1
	v_bitop3_b32 v56, v56, s5, v13 bitop3:0xe4
	v_bfe_i32 v13, v10, 1, 1
	v_bitop3_b32 v69, v69, s5, v13 bitop3:0xe4
	v_bfe_i32 v13, v10, 17, 1
	v_bitop3_b32 v65, v65, s5, v13 bitop3:0xe4
	v_bfe_i32 v13, v11, 1, 1
	v_bitop3_b32 v61, v61, s5, v13 bitop3:0xe4
	v_bfe_i32 v13, v11, 17, 1
	v_bitop3_b32 v57, v57, s5, v13 bitop3:0xe4
	v_bfe_i32 v13, v10, 2, 1
	v_bitop3_b32 v70, v70, s5, v13 bitop3:0xe4
	v_bfe_i32 v13, v10, 18, 1
	v_bitop3_b32 v66, v66, s5, v13 bitop3:0xe4
	v_bfe_i32 v13, v11, 2, 1
	v_bitop3_b32 v62, v62, s5, v13 bitop3:0xe4
	v_bfe_i32 v13, v11, 18, 1
	v_bitop3_b32 v58, v58, s5, v13 bitop3:0xe4
	v_bfe_i32 v13, v10, 3, 1
	v_bfe_i32 v10, v10, 19, 1
	v_bitop3_b32 v67, v67, s5, v10 bitop3:0xe4
	v_bfe_i32 v10, v11, 3, 1
	v_bitop3_b32 v63, v63, s5, v10 bitop3:0xe4
	v_bfe_i32 v10, v11, 19, 1
	v_bitop3_b32 v71, v71, s5, v13 bitop3:0xe4
	v_bitop3_b32 v59, v59, s5, v10 bitop3:0xe4

.LBB1_44:
	v_exp_f32_e32 v10, v68
	v_exp_f32_e32 v11, v69
	v_exp_f32_e32 v32, v64
	v_exp_f32_e32 v13, v70
	v_exp_f32_e32 v31, v71
	v_cvt_pkrtz_f16_f32 v64, v10, v11
	ds_read_b128 v[72:75], v87 offset:8192
	ds_read_b128 v[76:79], v87 offset:10240
	v_exp_f32_e32 v33, v65
	v_exp_f32_e32 v54, v66
	v_exp_f32_e32 v55, v67
	ds_read_b128 v[80:83], v87 offset:12288
	ds_read_b128 v[106:109], v87 offset:9216
	v_cvt_pkrtz_f16_f32 v65, v13, v31
	v_cvt_pkrtz_f16_f32 v67, v54, v55
	v_cvt_pkrtz_f16_f32 v66, v32, v33
	v_exp_f32_e32 v84, v60
	v_exp_f32_e32 v85, v61
	v_exp_f32_e32 v11, v62
	s_waitcnt lgkmcnt(3)
	v_mfma_f32_16x16x32_f16 v[46:49], v[72:75], v[64:67], v[46:49]
	v_exp_f32_e32 v13, v63
	ds_read_b128 v[60:63], v87 offset:14336
	ds_read_b128 v[110:113], v87 offset:11264
	v_exp_f32_e32 v31, v56
	s_waitcnt lgkmcnt(4)
	v_mfma_f32_16x16x32_f16 v[42:45], v[76:79], v[64:67], v[42:45]
	v_exp_f32_e32 v72, v57
	ds_read_b128 v[54:57], v87 offset:13312
	v_exp_f32_e32 v73, v58
	s_waitcnt lgkmcnt(4)
	v_mfma_f32_16x16x32_f16 v[38:41], v[80:83], v[64:67], v[38:41]
	ds_read_b128 v[78:81], v87 offset:15360
	v_exp_f32_e32 v74, v59
	v_cvt_pkrtz_f16_f32 v58, v84, v85
	v_mfma_f32_16x16x32_f16 v[50:53], v[114:117], v[64:67], v[50:53]
	v_cvt_pkrtz_f16_f32 v59, v11, v13
	s_waitcnt lgkmcnt(3)
	v_mfma_f32_16x16x32_f16 v[34:37], v[60:63], v[64:67], v[34:37]
	v_cvt_pkrtz_f16_f32 v61, v73, v74
	v_cvt_pkrtz_f16_f32 v60, v31, v72
	s_nop 1
	v_mfma_f32_16x16x32_f16 v[50:53], v[114:117], v[58:61], v[50:53]
	v_mfma_f32_16x16x32_f16 v[46:49], v[106:109], v[58:61], v[46:49]
	s_waitcnt lgkmcnt(2)
	v_mfma_f32_16x16x32_f16 v[42:45], v[110:113], v[58:61], v[42:45]
	s_waitcnt lgkmcnt(1)
	v_mfma_f32_16x16x32_f16 v[38:41], v[54:57], v[58:61], v[38:41]
	s_waitcnt lgkmcnt(0)
	v_mfma_f32_16x16x32_f16 v[34:37], v[78:81], v[58:61], v[34:37]
	s_andn2_b64 vcc, exec, s[18:19]
	s_cbranch_vccnz .Lat_exit4
	s_waitcnt vmcnt(0)
	v_mov_b64_e32 v[102:103], v[100:101]
	ds_write_b128 v99, v[22:25] offset:16384
	ds_write_b128 v90, v[14:17] offset:24576
	ds_write_b128 v99, v[18:21] offset:20480
	ds_write_b128 v90, v[26:29] offset:28672
	s_mov_b64 s[14:15], s[0:1]
	s_mov_b32 s0, s16
	s_cmp_gt_i32 s11, 3
	s_cbranch_scc1 .LBB1_17
	s_branch .LBB1_20

.LBB1_27_b:
	s_lshl_b32 s13, 1, s0
	s_and_b32 s0, s13, s4
	s_cmp_eq_u32 s0, 0
	s_cbranch_scc1 .LBB1_32_b
	ds_read_b128 v[58:61], v124 offset:16384
	ds_read_b128 v[62:65], v91 offset:16384
	v_lshrrev_b64 v[10:11], v98, v[102:103]
	v_bfe_i32 v13, v10, 1, 1
	v_bfe_i32 v31, v10, 2, 1
	s_waitcnt lgkmcnt(1)
	v_mfma_f32_16x16x32_f16 v[58:61], v[58:61], v[2:5], v[120:123]
	v_bfe_i32 v32, v10, 3, 1
	v_bfe_i32 v11, v10, 0, 1
	s_waitcnt lgkmcnt(0)
	v_mfma_f32_16x16x32_f16 v[58:61], v[62:65], v[6:9], v[58:61]
	s_nop 7
	v_bitop3_b32 v10, v59, s5, v13 bitop3:0xe4
	v_bitop3_b32 v31, v60, s5, v31 bitop3:0xe4
	v_bitop3_b32 v13, v61, s5, v32 bitop3:0xe4
	v_max_f32_e32 v32, v13, v13
	v_max_f32_e32 v33, v31, v31
	v_bitop3_b32 v11, v58, s5, v11 bitop3:0xe4
	v_max_f32_e32 v32, v33, v32
	v_max3_f32 v32, v11, v10, v32
	v_cmp_lt_f32_e32 vcc, s7, v32
	s_or_b64 s[0:1], s[14:15], vcc
	s_cbranch_scc0 .LBB1_35_b
	v_and_b32_e32 v58, 64, v0
	v_xor_b32_e32 v33, 16, v0
	v_add_u32_e32 v58, 64, v58
	v_cmp_lt_i32_e32 vcc, v33, v58
	s_mov_b64 s[22:23], 0
	s_nop 0
	v_cndmask_b32_e32 v33, v0, v33, vcc
	v_lshlrev_b32_e32 v33, 2, v33
	ds_bpermute_b32 v33, v33, v32
	v_max_f32_e32 v32, v32, v32
	s_waitcnt lgkmcnt(0)
	v_max_f32_e32 v33, v33, v33
	v_max_f32_e32 v32, v32, v33
	v_mov_b32_e32 v33, v32
	s_nop 1
	v_permlane32_swap_b32_e32 v32, v33
	v_max_f32_e32 v33, v33, v33
	v_max_f32_e32 v32, v32, v32
	v_max_f32_e32 v32, v32, v33
	v_cmp_nlg_f32_e32 vcc, s5, v32
	v_cmp_lg_f32_e64 s[0:1], s5, v32
	s_and_saveexec_b64 s[24:25], s[0:1]
	v_cmp_lt_f32_e64 s[0:1], s7, v32
	s_or_b64 s[0:1], s[14:15], s[0:1]
	s_and_b64 s[22:23], s[0:1], exec
	s_or_b64 exec, exec, s[24:25]
	v_exp_f32_e64 v33, -v32
	v_cndmask_b32_e64 v32, 0, v32, s[22:23]
	v_sub_f32_e32 v11, v11, v32
	v_sub_f32_e32 v10, v10, v32
	v_cndmask_b32_e64 v33, v33, 1.0, s[14:15]
	v_cndmask_b32_e64 v66, 1.0, v33, s[22:23]
	v_pk_mul_f32 v[60:61], v[48:49], v[66:67] op_sel_hi:[1,0]
	v_pk_mul_f32 v[58:59], v[46:47], v[66:67] op_sel_hi:[1,0]
	v_pk_mul_f32 v[64:65], v[66:67], v[44:45] op_sel_hi:[0,1]
	v_pk_mul_f32 v[62:63], v[66:67], v[42:43] op_sel_hi:[0,1]
	v_pk_mul_f32 v[80:81], v[66:67], v[40:41] op_sel_hi:[0,1]
	v_pk_mul_f32 v[78:79], v[66:67], v[38:39] op_sel_hi:[0,1]
	v_pk_mul_f32 v[84:85], v[66:67], v[36:37] op_sel_hi:[0,1]
	v_pk_mul_f32 v[82:83], v[66:67], v[34:35] op_sel_hi:[0,1]
	v_pk_mul_f32 v[68:69], v[52:53], v[66:67] op_sel_hi:[1,0]
	v_pk_mul_f32 v[66:67], v[50:51], v[66:67] op_sel_hi:[1,0]
	v_sub_f32_e32 v31, v31, v32
	v_sub_f32_e32 v13, v13, v32
	v_sub_f32_e32 v120, v120, v32
	v_sub_f32_e32 v121, v121, v32
	v_sub_f32_e32 v122, v122, v32
	v_sub_f32_e32 v123, v123, v32
	s_and_b64 s[0:1], s[14:15], vcc
	s_branch .LBB1_36_b

.LBB1_34_b:
	s_waitcnt vmcnt(0)
	v_mov_b64_e32 v[102:103], v[100:101]
	ds_write_b128 v99, v[22:25]
	ds_write_b128 v90, v[14:17] offset:8192
	ds_write_b128 v99, v[18:21] offset:4096
	ds_write_b128 v90, v[26:29] offset:12288
	s_cbranch_execnz .LBB1_46_b
	s_branch .LBB1_47

.LBB1_36_b:
	v_exp_f32_e32 v31, v31
	v_exp_f32_e32 v13, v13
	ds_read_b128 v[70:73], v87 offset:24576
	v_exp_f32_e32 v74, v11
	v_exp_f32_e32 v10, v10
	v_cvt_pkrtz_f16_f32 v11, v31, v13
	v_cvt_pkrtz_f16_f32 v10, v74, v10
	v_mov_b32_e32 v13, v12
	ds_read_b128 v[108:111], v87 offset:30720
	s_nop 0
	v_mfma_f32_16x16x32_f16 v[74:77], v[114:117], v[10:13], v[66:69]
	s_nop 2
	ds_read_b128 v[66:69], v87 offset:26624
	s_waitcnt lgkmcnt(2)
	v_mfma_f32_16x16x32_f16 v[70:73], v[70:73], v[10:13], v[58:61]
	s_nop 2
	ds_read_b128 v[58:61], v87 offset:28672
	s_waitcnt lgkmcnt(1)
	v_mfma_f32_16x16x32_f16 v[66:69], v[66:69], v[10:13], v[62:65]
	s_waitcnt lgkmcnt(0)
	v_mfma_f32_16x16x32_f16 v[62:65], v[58:61], v[10:13], v[78:81]
	v_mfma_f32_16x16x32_f16 v[58:61], v[108:111], v[10:13], v[82:85]
	s_branch .LBB1_33_b
.LBB1_37_b:
	ds_read_b128 v[58:61], v124 offset:16384
	ds_read_b128 v[62:65], v124 offset:18432
	ds_read_b128 v[66:69], v91 offset:16384
	ds_read_b128 v[72:75], v91 offset:18432
	s_and_b32 s0, s13, s6
	s_waitcnt lgkmcnt(3)
	v_mfma_f32_16x16x32_f16 v[58:61], v[58:61], v[2:5], v[120:123]
	s_cmp_lg_u32 s0, 0
	s_waitcnt lgkmcnt(2)
	v_mfma_f32_16x16x32_f16 v[62:65], v[62:65], v[2:5], v[120:123]
	s_waitcnt lgkmcnt(1)
	v_mfma_f32_16x16x32_f16 v[68:71], v[66:69], v[6:9], v[58:61]
	s_waitcnt lgkmcnt(0)
	v_mfma_f32_16x16x32_f16 v[64:67], v[72:75], v[6:9], v[62:65]
	s_nop 0
	ds_read_b128 v[58:61], v124 offset:20480
	ds_read_b128 v[72:75], v124 offset:22528
	ds_read_b128 v[76:79], v91 offset:20480
	ds_read_b128 v[80:83], v91 offset:22528
	s_waitcnt lgkmcnt(3)
	v_mfma_f32_16x16x32_f16 v[58:61], v[58:61], v[2:5], v[120:123]
	s_waitcnt lgkmcnt(1)
	v_mfma_f32_16x16x32_f16 v[60:63], v[76:79], v[6:9], v[58:61]
	v_mfma_f32_16x16x32_f16 v[56:59], v[72:75], v[2:5], v[120:123]
	s_waitcnt lgkmcnt(0)
	v_mfma_f32_16x16x32_f16 v[56:59], v[80:83], v[6:9], v[56:59]
	s_cbranch_scc1 .LBB1_39_b
	v_lshrrev_b64 v[10:11], v98, v[102:103]
	v_bfe_i32 v13, v10, 0, 1
	v_bitop3_b32 v68, v68, s5, v13 bitop3:0xe4
	v_bfe_i32 v13, v10, 16, 1
	v_bitop3_b32 v64, v64, s5, v13 bitop3:0xe4
	v_bfe_i32 v13, v11, 0, 1
	v_bitop3_b32 v60, v60, s5, v13 bitop3:0xe4
	v_bfe_i32 v13, v11, 16, 1
	v_bitop3_b32 v56, v56, s5, v13 bitop3:0xe4
	v_bfe_i32 v13, v10, 1, 1
	v_bitop3_b32 v69, v69, s5, v13 bitop3:0xe4
	v_bfe_i32 v13, v10, 17, 1
	v_bitop3_b32 v65, v65, s5, v13 bitop3:0xe4
	v_bfe_i32 v13, v11, 1, 1
	v_bitop3_b32 v61, v61, s5, v13 bitop3:0xe4
	v_bfe_i32 v13, v11, 17, 1
	v_bitop3_b32 v57, v57, s5, v13 bitop3:0xe4
	v_bfe_i32 v13, v10, 2, 1
	v_bitop3_b32 v70, v70, s5, v13 bitop3:0xe4
	v_bfe_i32 v13, v10, 18, 1
	v_bitop3_b32 v66, v66, s5, v13 bitop3:0xe4
	v_bfe_i32 v13, v11, 2, 1
	v_bitop3_b32 v62, v62, s5, v13 bitop3:0xe4
	v_bfe_i32 v13, v11, 18, 1
	v_bitop3_b32 v58, v58, s5, v13 bitop3:0xe4
	v_bfe_i32 v13, v10, 3, 1
	v_bfe_i32 v10, v10, 19, 1
	v_bitop3_b32 v67, v67, s5, v10 bitop3:0xe4
	v_bfe_i32 v10, v11, 3, 1
	v_bitop3_b32 v63, v63, s5, v10 bitop3:0xe4
	v_bfe_i32 v10, v11, 19, 1
	v_bitop3_b32 v71, v71, s5, v13 bitop3:0xe4
	v_bitop3_b32 v59, v59, s5, v10 bitop3:0xe4

.LBB1_44_b:
	v_exp_f32_e32 v10, v68
	v_exp_f32_e32 v11, v69
	v_exp_f32_e32 v32, v64
	v_exp_f32_e32 v13, v70
	v_exp_f32_e32 v31, v71
	v_cvt_pkrtz_f16_f32 v64, v10, v11
	ds_read_b128 v[72:75], v87 offset:24576
	ds_read_b128 v[76:79], v87 offset:26624
	v_exp_f32_e32 v33, v65
	v_exp_f32_e32 v54, v66
	v_exp_f32_e32 v55, v67
	ds_read_b128 v[80:83], v87 offset:28672
	ds_read_b128 v[106:109], v87 offset:25600
	v_cvt_pkrtz_f16_f32 v65, v13, v31
	v_cvt_pkrtz_f16_f32 v67, v54, v55
	v_cvt_pkrtz_f16_f32 v66, v32, v33
	v_exp_f32_e32 v84, v60
	v_exp_f32_e32 v85, v61
	v_exp_f32_e32 v11, v62
	s_waitcnt lgkmcnt(3)
	v_mfma_f32_16x16x32_f16 v[46:49], v[72:75], v[64:67], v[46:49]
	v_exp_f32_e32 v13, v63
	ds_read_b128 v[60:63], v87 offset:30720
	ds_read_b128 v[110:113], v87 offset:27648
	v_exp_f32_e32 v31, v56
	s_waitcnt lgkmcnt(4)
	v_mfma_f32_16x16x32_f16 v[42:45], v[76:79], v[64:67], v[42:45]
	v_exp_f32_e32 v72, v57
	ds_read_b128 v[54:57], v87 offset:29696
	v_exp_f32_e32 v73, v58
	s_waitcnt lgkmcnt(4)
	v_mfma_f32_16x16x32_f16 v[38:41], v[80:83], v[64:67], v[38:41]
	ds_read_b128 v[78:81], v87 offset:31744
	v_exp_f32_e32 v74, v59
	v_cvt_pkrtz_f16_f32 v58, v84, v85
	v_mfma_f32_16x16x32_f16 v[50:53], v[114:117], v[64:67], v[50:53]
	v_cvt_pkrtz_f16_f32 v59, v11, v13
	s_waitcnt lgkmcnt(3)
	v_mfma_f32_16x16x32_f16 v[34:37], v[60:63], v[64:67], v[34:37]
	v_cvt_pkrtz_f16_f32 v61, v73, v74
	v_cvt_pkrtz_f16_f32 v60, v31, v72
	s_nop 1
	v_mfma_f32_16x16x32_f16 v[50:53], v[114:117], v[58:61], v[50:53]
	v_mfma_f32_16x16x32_f16 v[46:49], v[106:109], v[58:61], v[46:49]
	s_waitcnt lgkmcnt(2)
	v_mfma_f32_16x16x32_f16 v[42:45], v[110:113], v[58:61], v[42:45]
	s_waitcnt lgkmcnt(1)
	v_mfma_f32_16x16x32_f16 v[38:41], v[54:57], v[58:61], v[38:41]
	s_waitcnt lgkmcnt(0)
	v_mfma_f32_16x16x32_f16 v[34:37], v[78:81], v[58:61], v[34:37]
	s_andn2_b64 vcc, exec, s[18:19]
	s_cbranch_vccnz .Lat_exit4_b
	s_waitcnt vmcnt(0)
	v_mov_b64_e32 v[102:103], v[100:101]
	ds_write_b128 v99, v[22:25]
	ds_write_b128 v90, v[14:17] offset:8192
	ds_write_b128 v99, v[18:21] offset:4096
	ds_write_b128 v90, v[26:29] offset:12288
	s_mov_b64 s[14:15], s[0:1]
	s_mov_b32 s0, s16
	s_cmp_gt_i32 s11, 3
	s_cbranch_scc1 .LBB1_17
	s_branch .LBB1_20

	.amdhsa_kernel _Z11attn_kernelPKDF16_S0_S0_PKyPKiPDF16_
		.amdhsa_group_segment_fixed_size 36864
		.amdhsa_private_segment_fixed_size 0
		.amdhsa_kernarg_size 48
		.amdhsa_user_sgpr_count 2
		.amdhsa_user_sgpr_dispatch_ptr 0
		.amdhsa_user_sgpr_queue_ptr 0
		.amdhsa_user_sgpr_kernarg_segment_ptr 1
		.amdhsa_user_sgpr_dispatch_id 0
		.amdhsa_user_sgpr_kernarg_preload_length 0
		.amdhsa_user_sgpr_kernarg_preload_offset 0
		.amdhsa_user_sgpr_private_segment_size 0
		.amdhsa_uses_dynamic_stack 0
		.amdhsa_enable_private_segment 0
		.amdhsa_system_sgpr_workgroup_id_x 1
		.amdhsa_system_sgpr_workgroup_id_y 0
		.amdhsa_system_sgpr_workgroup_id_z 0
		.amdhsa_system_sgpr_workgroup_info 0
		.amdhsa_system_vgpr_workitem_id 0
		.amdhsa_next_free_vgpr 125
		.amdhsa_next_free_sgpr 96
		.amdhsa_accum_offset 128
		.amdhsa_reserve_vcc 1
		.amdhsa_float_round_mode_32 0
		.amdhsa_float_round_mode_16_64 0
		.amdhsa_float_denorm_mode_32 3
		.amdhsa_float_denorm_mode_16_64 3
		.amdhsa_dx10_clamp 1
		.amdhsa_ieee_mode 1
		.amdhsa_fp16_overflow 0
		.amdhsa_tg_split 0
		.amdhsa_exception_fp_ieee_invalid_op 0
		.amdhsa_exception_fp_denorm_src 0
		.amdhsa_exception_fp_ieee_div_zero 0
		.amdhsa_exception_fp_ieee_overflow 0
		.amdhsa_exception_fp_ieee_underflow 0
		.amdhsa_exception_fp_ieee_inexact 0
		.amdhsa_exception_int_div_zero 0
	.end_amdhsa_kernel

amdhsa.kernels:
  - .agpr_count:     0
    .args:
      - .actual_access:  read_only
        .address_space:  global
        .offset:         0
        .size:           8
        .value_kind:     global_buffer
      - .actual_access:  read_only
        .address_space:  global
        .offset:         8
        .size:           8
        .value_kind:     global_buffer
      - .actual_access:  read_only
        .address_space:  global
        .offset:         16
        .size:           8
        .value_kind:     global_buffer
      - .actual_access:  read_only
        .address_space:  global
        .offset:         24
        .size:           8
        .value_kind:     global_buffer
      - .actual_access:  read_only
        .address_space:  global
        .offset:         32
        .size:           8
        .value_kind:     global_buffer
      - .actual_access:  read_only
        .address_space:  global
        .offset:         40
        .size:           8
        .value_kind:     global_buffer
      - .actual_access:  write_only
        .address_space:  global
        .offset:         48
        .size:           8
        .value_kind:     global_buffer
      - .actual_access:  write_only
        .address_space:  global
        .offset:         56
        .size:           8
        .value_kind:     global_buffer
      - .actual_access:  write_only
        .address_space:  global
        .offset:         64
        .size:           8
        .value_kind:     global_buffer
      - .actual_access:  write_only
        .address_space:  global
        .offset:         72
        .size:           8
        .value_kind:     global_buffer
      - .actual_access:  write_only
        .address_space:  global
        .offset:         80
        .size:           8
        .value_kind:     global_buffer
    .group_segment_fixed_size: 16640
    .kernarg_segment_align: 8
    .kernarg_segment_size: 88
    .language:       OpenCL C
    .language_version:
      - 2
      - 0
    .max_flat_workgroup_size: 256
    .name:           _Z11prep_kernelPKfS0_S0_S0_S0_PKiPDF16_S3_S3_PyPi
    .private_segment_fixed_size: 0
    .sgpr_count:     54
    .sgpr_spill_count: 0
    .symbol:         _Z11prep_kernelPKfS0_S0_S0_S0_PKiPDF16_S3_S3_PyPi.kd
    .uniform_work_group_size: 1
    .uses_dynamic_stack: false
    .vgpr_count:     46
    .vgpr_spill_count: 0
    .wavefront_size: 64
  - .agpr_count:     0
    .args:
      - .actual_access:  read_only
        .address_space:  global
        .offset:         0
        .size:           8
        .value_kind:     global_buffer
      - .actual_access:  read_only
        .address_space:  global
        .offset:         8
        .size:           8
        .value_kind:     global_buffer
      - .actual_access:  read_only
        .address_space:  global
        .offset:         16
        .size:           8
        .value_kind:     global_buffer
      - .actual_access:  read_only
        .address_space:  global
        .offset:         24
        .size:           8
        .value_kind:     global_buffer
      - .actual_access:  read_only
        .address_space:  global
        .offset:         32
        .size:           8
        .value_kind:     global_buffer
      - .actual_access:  write_only
        .address_space:  global
        .offset:         40
        .size:           8
        .value_kind:     global_buffer
    .group_segment_fixed_size: 36864
    .kernarg_segment_align: 8
    .kernarg_segment_size: 48
    .language:       OpenCL C
    .language_version:
      - 2
      - 0
    .max_flat_workgroup_size: 256
    .name:           _Z11attn_kernelPKDF16_S0_S0_PKyPKiPDF16_
    .private_segment_fixed_size: 0
    .sgpr_count:     32
    .sgpr_spill_count: 0
    .symbol:         _Z11attn_kernelPKDF16_S0_S0_PKyPKiPDF16_.kd
    .uniform_work_group_size: 1
    .uses_dynamic_stack: false
    .vgpr_count:     125
    .vgpr_spill_count: 0
    .wavefront_size: 64
  - .agpr_count:     0
    .args:
      - .address_space:  global
        .offset:         0
        .size:           8
        .value_kind:     global_buffer
      - .address_space:  global
        .offset:         8
        .size:           8
        .value_kind:     global_buffer
      - .actual_access:  read_only
        .address_space:  global
        .offset:         16
        .size:           8
        .value_kind:     global_buffer
      - .actual_access:  read_only
        .address_space:  global
        .offset:         24
        .size:           8
        .value_kind:     global_buffer
      - .actual_access:  read_only
        .address_space:  global
        .offset:         32
        .size:           8
        .value_kind:     global_buffer
      - .actual_access:  read_only
        .address_space:  global
        .offset:         40
        .size:           8
        .value_kind:     global_buffer
      - .actual_access:  write_only
        .address_space:  global
        .offset:         48
        .size:           8
        .value_kind:     global_buffer
      - .actual_access:  write_only
        .address_space:  global
        .offset:         56
        .size:           8
        .value_kind:     global_buffer
      - .actual_access:  write_only
        .address_space:  global
        .offset:         64
        .size:           8
        .value_kind:     global_buffer
    .group_segment_fixed_size: 114688
    .kernarg_segment_align: 8
    .kernarg_segment_size: 72
    .language:       OpenCL C
    .language_version:
      - 2
      - 0
    .max_flat_workgroup_size: 512
    .name:           _Z9gemm_gldsILi256ELi192ELi4ELi2ELi2ELi4ELi8ELi0ELi4096ELi3072ELi1024EEvPKDF16_S1_PfPKfS4_PKiPDF16_S7_S7_
    .private_segment_fixed_size: 0
    .sgpr_count:     29
    .sgpr_spill_count: 0
    .symbol:         _Z9gemm_gldsILi256ELi192ELi4ELi2ELi2ELi4ELi8ELi0ELi4096ELi3072ELi1024EEvPKDF16_S1_PfPKfS4_PKiPDF16_S7_S7_.kd
    .uniform_work_group_size: 1
    .uses_dynamic_stack: false
    .vgpr_count:     214
    .vgpr_spill_count: 0
    .wavefront_size: 64
  - .agpr_count:     0
    .args:
      - .address_space:  global
        .offset:         0
        .size:           8
        .value_kind:     global_buffer
      - .address_space:  global
        .offset:         8
        .size:           8
        .value_kind:     global_buffer
      - .actual_access:  write_only
        .address_space:  global
        .offset:         16
        .size:           8
        .value_kind:     global_buffer
      - .actual_access:  read_only
        .address_space:  global
        .offset:         24
        .size:           8
        .value_kind:     global_buffer
      - .actual_access:  read_only
        .address_space:  global
        .offset:         32
        .size:           8
        .value_kind:     global_buffer
      - .actual_access:  read_only
        .address_space:  global
        .offset:         40
        .size:           8
        .value_kind:     global_buffer
      - .actual_access:  read_only
        .address_space:  global
        .offset:         48
        .size:           8
        .value_kind:     global_buffer
      - .actual_access:  read_only
        .address_space:  global
        .offset:         56
        .size:           8
        .value_kind:     global_buffer
      - .actual_access:  read_only
        .address_space:  global
        .offset:         64
        .size:           8
        .value_kind:     global_buffer
    .group_segment_fixed_size: 98304
    .kernarg_segment_align: 8
    .kernarg_segment_size: 72
    .language:       OpenCL C
    .language_version:
      - 2
      - 0
    .max_flat_workgroup_size: 512
    .name:           _Z9gemm_gldsILi128ELi128ELi4ELi2ELi3ELi8ELi4ELi1ELi4096ELi1024ELi1024EEvPKDF16_S1_PfPKfS4_PKiPDF16_S7_S7_
    .private_segment_fixed_size: 0
    .sgpr_count:     20
    .sgpr_spill_count: 0
    .symbol:         _Z9gemm_gldsILi128ELi128ELi4ELi2ELi3ELi8ELi4ELi1ELi4096ELi1024ELi1024EEvPKDF16_S1_PfPKfS4_PKiPDF16_S7_S7_.kd
    .uniform_work_group_size: 1
    .uses_dynamic_stack: false
    .vgpr_count:     92
    .vgpr_spill_count: 0
    .wavefront_size: 64
